# speedup vs baseline: 1.0203x; 1.0058x over previous
.Ltile0:
	s_mov_b32 s34, 0
	s_waitcnt vmcnt(5)
	s_waitcnt lgkmcnt(0)
	s_barrier
	s_mul_i32 s35, s33, 0xa000
	v_add_u32_e32 v240, s35, v222
	v_add_u32_e32 v241, s35, v223
	v_add_u32_e32 v242, s35, v224
	s_add_u32 s33, s33, 1
	s_cmp_eq_u32 s33, 3
	s_cselect_b32 s33, 0, s33
	ds_read_b128 v[244:247], v240 offset:6144
	ds_read_b128 v[252:255], v240 offset:7168
	v_mfma_scale_f32_16x16x128_f8f6f4 v[0:3], v[128:131], v[160:165], 0, v208, v216 op_sel_hi:[0,0,0] cbsz:4 blgp:2
	s_cmp_eq_u32 s34, 13
	v_mfma_scale_f32_16x16x128_f8f6f4 v[4:7], v[128:131], v[166:171], 0, v208, v217 op_sel_hi:[0,0,0] cbsz:4 blgp:2
	s_cselect_b32 s36, s38, s36
	v_mfma_scale_f32_16x16x128_f8f6f4 v[8:11], v[128:131], v[172:177], 0, v208, v218 op_sel_hi:[0,0,0] cbsz:4 blgp:2
	s_cselect_b32 s37, s39, s37
	v_mfma_scale_f32_16x16x128_f8f6f4 v[12:15], v[128:131], v[178:183], 0, v208, v219 op_sel_hi:[0,0,0] cbsz:4 blgp:2
	s_mov_b32 m0, s40
	v_mfma_scale_f32_16x16x128_f8f6f4 v[16:19], v[132:135], v[160:165], 0, v209, v216 op_sel_hi:[0,0,0] cbsz:4 blgp:2
	ds_read_b128 v[184:187], v241 offset:0
	v_mfma_scale_f32_16x16x128_f8f6f4 v[20:23], v[132:135], v[166:171], 0, v209, v217 op_sel_hi:[0,0,0] cbsz:4 blgp:2
	buffer_load_dwordx4 v221, s[4:7], s36 offen lds
	v_mfma_scale_f32_16x16x128_f8f6f4 v[24:27], v[132:135], v[172:177], 0, v209, v218 op_sel_hi:[0,0,0] cbsz:4 blgp:2
	s_add_u32 m0, s40, 0x2000
	v_mfma_scale_f32_16x16x128_f8f6f4 v[28:31], v[132:135], v[178:183], 0, v209, v219 op_sel_hi:[0,0,0] cbsz:4 blgp:2
	ds_read_b64 v[188:189], v242 offset:0
	v_mfma_scale_f32_16x16x128_f8f6f4 v[32:35], v[136:139], v[160:165], 0, v210, v216 op_sel_hi:[0,0,0] cbsz:4 blgp:2
	buffer_load_dwordx4 v225, s[4:7], s36 offen lds
	v_mfma_scale_f32_16x16x128_f8f6f4 v[36:39], v[136:139], v[166:171], 0, v210, v217 op_sel_hi:[0,0,0] cbsz:4 blgp:2
	s_add_u32 m0, s40, 0x4000
	v_mfma_scale_f32_16x16x128_f8f6f4 v[40:43], v[136:139], v[172:177], 0, v210, v218 op_sel_hi:[0,0,0] cbsz:4 blgp:2
	ds_read_b128 v[190:193], v241 offset:1536
	v_mfma_scale_f32_16x16x128_f8f6f4 v[44:47], v[136:139], v[178:183], 0, v210, v219 op_sel_hi:[0,0,0] cbsz:4 blgp:2
	buffer_load_dwordx4 v221, s[4:7], s37 offen lds
	v_mfma_scale_f32_16x16x128_f8f6f4 v[48:51], v[140:143], v[160:165], 0, v211, v216 op_sel_hi:[0,0,0] cbsz:4 blgp:2
	s_add_u32 m0, s40, 0x6000
	v_mfma_scale_f32_16x16x128_f8f6f4 v[52:55], v[140:143], v[166:171], 0, v211, v217 op_sel_hi:[0,0,0] cbsz:4 blgp:2
	ds_read_b64 v[194:195], v242 offset:1536
	v_mfma_scale_f32_16x16x128_f8f6f4 v[56:59], v[140:143], v[172:177], 0, v211, v218 op_sel_hi:[0,0,0] cbsz:4 blgp:2
	buffer_load_dwordx4 v225, s[4:7], s37 offen lds
	v_mfma_scale_f32_16x16x128_f8f6f4 v[60:63], v[140:143], v[178:183], 0, v211, v219 op_sel_hi:[0,0,0] cbsz:4 blgp:2
	s_add_u32 m0, s40, 0x8000
	v_mfma_scale_f32_16x16x128_f8f6f4 v[64:67], v[144:147], v[160:165], 0, v212, v216 op_sel_hi:[0,0,0] cbsz:4 blgp:2
	ds_read_b128 v[196:199], v241 offset:3072
	v_mfma_scale_f32_16x16x128_f8f6f4 v[68:71], v[144:147], v[166:171], 0, v212, v217 op_sel_hi:[0,0,0] cbsz:4 blgp:2
	buffer_load_dwordx4 v226, s[4:7], s37 offen lds
	v_mfma_scale_f32_16x16x128_f8f6f4 v[72:75], v[144:147], v[172:177], 0, v212, v218 op_sel_hi:[0,0,0] cbsz:4 blgp:2
	ds_read_b64 v[200:201], v242 offset:3072
	v_mfma_scale_f32_16x16x128_f8f6f4 v[76:79], v[144:147], v[178:183], 0, v212, v219 op_sel_hi:[0,0,0] cbsz:4 blgp:2
	ds_read_b128 v[202:205], v241 offset:4608
	v_mfma_scale_f32_16x16x128_f8f6f4 v[80:83], v[148:151], v[160:165], 0, v213, v216 op_sel_hi:[0,0,0] cbsz:4 blgp:2
	ds_read_b64 v[206:207], v242 offset:4608
	v_mfma_scale_f32_16x16x128_f8f6f4 v[84:87], v[148:151], v[166:171], 0, v213, v217 op_sel_hi:[0,0,0] cbsz:4 blgp:2
	s_add_u32 s36, s36, 0x4000
	v_mfma_scale_f32_16x16x128_f8f6f4 v[88:91], v[148:151], v[172:177], 0, v213, v218 op_sel_hi:[0,0,0] cbsz:4 blgp:2
	s_add_u32 s37, s37, 0x6000
	v_mfma_scale_f32_16x16x128_f8f6f4 v[92:95], v[148:151], v[178:183], 0, v213, v219 op_sel_hi:[0,0,0] cbsz:4 blgp:2
	s_add_u32 s40, s40, 0xa000
	v_mfma_scale_f32_16x16x128_f8f6f4 v[96:99], v[152:155], v[160:165], 0, v214, v216 op_sel_hi:[0,0,0] cbsz:4 blgp:2
	s_sub_u32 s41, s40, 0x1e000
	v_mfma_scale_f32_16x16x128_f8f6f4 v[100:103], v[152:155], v[166:171], 0, v214, v217 op_sel_hi:[0,0,0] cbsz:4 blgp:2
	s_cmp_ge_u32 s40, s49
	v_mfma_scale_f32_16x16x128_f8f6f4 v[104:107], v[152:155], v[172:177], 0, v214, v218 op_sel_hi:[0,0,0] cbsz:4 blgp:2
	s_cselect_b32 s40, s41, s40
	v_mfma_scale_f32_16x16x128_f8f6f4 v[108:111], v[152:155], v[178:183], 0, v214, v219 op_sel_hi:[0,0,0] cbsz:4 blgp:2
	ds_read_b128 v[128:131], v240 offset:0
	v_mfma_scale_f32_16x16x128_f8f6f4 v[112:115], v[156:159], v[160:165], 0, v215, v216 op_sel_hi:[0,0,0] cbsz:4 blgp:2
	ds_read_b128 v[132:135], v240 offset:1024
	v_mfma_scale_f32_16x16x128_f8f6f4 v[116:119], v[156:159], v[166:171], 0, v215, v217 op_sel_hi:[0,0,0] cbsz:4 blgp:2
	ds_read_b128 v[136:139], v240 offset:2048
	v_mfma_scale_f32_16x16x128_f8f6f4 v[120:123], v[156:159], v[172:177], 0, v215, v218 op_sel_hi:[0,0,0] cbsz:4 blgp:2
	ds_read_b128 v[140:143], v240 offset:3072
	v_mfma_scale_f32_16x16x128_f8f6f4 v[124:127], v[156:159], v[178:183], 0, v215, v219 op_sel_hi:[0,0,0] cbsz:4 blgp:2
	ds_read_b128 v[144:147], v240 offset:4096
	ds_read_b128 v[148:151], v240 offset:5120
	s_add_u32 s34, s34, 1
	s_waitcnt vmcnt(5)
	s_waitcnt lgkmcnt(0)
	s_barrier
	s_mul_i32 s35, s33, 0xa000
	v_add_u32_e32 v240, s35, v222
	v_add_u32_e32 v241, s35, v223
	v_add_u32_e32 v242, s35, v224
	s_add_u32 s33, s33, 1
	s_cmp_eq_u32 s33, 3
	s_cselect_b32 s33, 0, s33
	ds_read_b128 v[152:155], v240 offset:6144
	ds_read_b128 v[156:159], v240 offset:7168
	v_mfma_scale_f32_16x16x128_f8f6f4 v[0:3], v[128:131], v[184:189], v[0:3], v208, v216 op_sel_hi:[0,0,0] cbsz:4 blgp:2
	s_cmp_eq_u32 s34, 13
	v_mfma_scale_f32_16x16x128_f8f6f4 v[4:7], v[128:131], v[190:195], v[4:7], v208, v217 op_sel_hi:[0,0,0] cbsz:4 blgp:2
	s_cselect_b32 s36, s38, s36
	v_mfma_scale_f32_16x16x128_f8f6f4 v[8:11], v[128:131], v[196:201], v[8:11], v208, v218 op_sel_hi:[0,0,0] cbsz:4 blgp:2
	s_cselect_b32 s37, s39, s37
	v_mfma_scale_f32_16x16x128_f8f6f4 v[12:15], v[128:131], v[202:207], v[12:15], v208, v219 op_sel_hi:[0,0,0] cbsz:4 blgp:2
	s_mov_b32 m0, s40
	v_mfma_scale_f32_16x16x128_f8f6f4 v[16:19], v[132:135], v[184:189], v[16:19], v209, v216 op_sel_hi:[0,0,0] cbsz:4 blgp:2
	ds_read_b128 v[160:163], v241 offset:0
	v_mfma_scale_f32_16x16x128_f8f6f4 v[20:23], v[132:135], v[190:195], v[20:23], v209, v217 op_sel_hi:[0,0,0] cbsz:4 blgp:2
	buffer_load_dwordx4 v221, s[4:7], s36 offen lds
	v_mfma_scale_f32_16x16x128_f8f6f4 v[24:27], v[132:135], v[196:201], v[24:27], v209, v218 op_sel_hi:[0,0,0] cbsz:4 blgp:2
	s_add_u32 m0, s40, 0x2000
	v_mfma_scale_f32_16x16x128_f8f6f4 v[28:31], v[132:135], v[202:207], v[28:31], v209, v219 op_sel_hi:[0,0,0] cbsz:4 blgp:2
	ds_read_b64 v[164:165], v242 offset:0
	v_mfma_scale_f32_16x16x128_f8f6f4 v[32:35], v[136:139], v[184:189], v[32:35], v210, v216 op_sel_hi:[0,0,0] cbsz:4 blgp:2
	buffer_load_dwordx4 v225, s[4:7], s36 offen lds
	v_mfma_scale_f32_16x16x128_f8f6f4 v[36:39], v[136:139], v[190:195], v[36:39], v210, v217 op_sel_hi:[0,0,0] cbsz:4 blgp:2
	s_add_u32 m0, s40, 0x4000
	v_mfma_scale_f32_16x16x128_f8f6f4 v[40:43], v[136:139], v[196:201], v[40:43], v210, v218 op_sel_hi:[0,0,0] cbsz:4 blgp:2
	ds_read_b128 v[166:169], v241 offset:1536
	v_mfma_scale_f32_16x16x128_f8f6f4 v[44:47], v[136:139], v[202:207], v[44:47], v210, v219 op_sel_hi:[0,0,0] cbsz:4 blgp:2
	buffer_load_dwordx4 v221, s[4:7], s37 offen lds
	v_mfma_scale_f32_16x16x128_f8f6f4 v[48:51], v[140:143], v[184:189], v[48:51], v211, v216 op_sel_hi:[0,0,0] cbsz:4 blgp:2
	s_add_u32 m0, s40, 0x6000
	v_mfma_scale_f32_16x16x128_f8f6f4 v[52:55], v[140:143], v[190:195], v[52:55], v211, v217 op_sel_hi:[0,0,0] cbsz:4 blgp:2
	ds_read_b64 v[170:171], v242 offset:1536
	v_mfma_scale_f32_16x16x128_f8f6f4 v[56:59], v[140:143], v[196:201], v[56:59], v211, v218 op_sel_hi:[0,0,0] cbsz:4 blgp:2
	buffer_load_dwordx4 v225, s[4:7], s37 offen lds
	v_mfma_scale_f32_16x16x128_f8f6f4 v[60:63], v[140:143], v[202:207], v[60:63], v211, v219 op_sel_hi:[0,0,0] cbsz:4 blgp:2
	s_add_u32 m0, s40, 0x8000
	v_mfma_scale_f32_16x16x128_f8f6f4 v[64:67], v[144:147], v[184:189], v[64:67], v212, v216 op_sel_hi:[0,0,0] cbsz:4 blgp:2
	ds_read_b128 v[172:175], v241 offset:3072
	v_mfma_scale_f32_16x16x128_f8f6f4 v[68:71], v[144:147], v[190:195], v[68:71], v212, v217 op_sel_hi:[0,0,0] cbsz:4 blgp:2
	buffer_load_dwordx4 v226, s[4:7], s37 offen lds
	v_mfma_scale_f32_16x16x128_f8f6f4 v[72:75], v[144:147], v[196:201], v[72:75], v212, v218 op_sel_hi:[0,0,0] cbsz:4 blgp:2
	ds_read_b64 v[176:177], v242 offset:3072
	v_mfma_scale_f32_16x16x128_f8f6f4 v[76:79], v[144:147], v[202:207], v[76:79], v212, v219 op_sel_hi:[0,0,0] cbsz:4 blgp:2
	ds_read_b128 v[178:181], v241 offset:4608
	v_mfma_scale_f32_16x16x128_f8f6f4 v[80:83], v[148:151], v[184:189], v[80:83], v213, v216 op_sel_hi:[0,0,0] cbsz:4 blgp:2
	ds_read_b64 v[182:183], v242 offset:4608
	v_mfma_scale_f32_16x16x128_f8f6f4 v[84:87], v[148:151], v[190:195], v[84:87], v213, v217 op_sel_hi:[0,0,0] cbsz:4 blgp:2
	s_add_u32 s36, s36, 0x4000
	v_mfma_scale_f32_16x16x128_f8f6f4 v[88:91], v[148:151], v[196:201], v[88:91], v213, v218 op_sel_hi:[0,0,0] cbsz:4 blgp:2
	s_add_u32 s37, s37, 0x6000
	v_mfma_scale_f32_16x16x128_f8f6f4 v[92:95], v[148:151], v[202:207], v[92:95], v213, v219 op_sel_hi:[0,0,0] cbsz:4 blgp:2
	s_add_u32 s40, s40, 0xa000
	v_mfma_scale_f32_16x16x128_f8f6f4 v[96:99], v[244:247], v[184:189], v[96:99], v214, v216 op_sel_hi:[0,0,0] cbsz:4 blgp:2
	s_sub_u32 s41, s40, 0x1e000
	v_mfma_scale_f32_16x16x128_f8f6f4 v[100:103], v[244:247], v[190:195], v[100:103], v214, v217 op_sel_hi:[0,0,0] cbsz:4 blgp:2
	s_cmp_ge_u32 s40, s49
	v_mfma_scale_f32_16x16x128_f8f6f4 v[104:107], v[244:247], v[196:201], v[104:107], v214, v218 op_sel_hi:[0,0,0] cbsz:4 blgp:2
	s_cselect_b32 s40, s41, s40
	v_mfma_scale_f32_16x16x128_f8f6f4 v[108:111], v[244:247], v[202:207], v[108:111], v214, v219 op_sel_hi:[0,0,0] cbsz:4 blgp:2
	ds_read_b128 v[128:131], v240 offset:0
	v_mfma_scale_f32_16x16x128_f8f6f4 v[112:115], v[252:255], v[184:189], v[112:115], v215, v216 op_sel_hi:[0,0,0] cbsz:4 blgp:2
	ds_read_b128 v[132:135], v240 offset:1024
	v_mfma_scale_f32_16x16x128_f8f6f4 v[116:119], v[252:255], v[190:195], v[116:119], v215, v217 op_sel_hi:[0,0,0] cbsz:4 blgp:2
	ds_read_b128 v[136:139], v240 offset:2048
	v_mfma_scale_f32_16x16x128_f8f6f4 v[120:123], v[252:255], v[196:201], v[120:123], v215, v218 op_sel_hi:[0,0,0] cbsz:4 blgp:2
	ds_read_b128 v[140:143], v240 offset:3072
	v_mfma_scale_f32_16x16x128_f8f6f4 v[124:127], v[252:255], v[202:207], v[124:127], v215, v219 op_sel_hi:[0,0,0] cbsz:4 blgp:2
	ds_read_b128 v[144:147], v240 offset:4096
	ds_read_b128 v[148:151], v240 offset:5120
	s_add_u32 s34, s34, 1
.Lkloop0:
	s_waitcnt vmcnt(5)
	s_waitcnt lgkmcnt(0)
	s_barrier
	s_mul_i32 s35, s33, 0xa000
	v_add_u32_e32 v240, s35, v222
	v_add_u32_e32 v241, s35, v223
	v_add_u32_e32 v242, s35, v224
	s_add_u32 s33, s33, 1
	s_cmp_eq_u32 s33, 3
	s_cselect_b32 s33, 0, s33
	ds_read_b128 v[244:247], v240 offset:6144
	ds_read_b128 v[252:255], v240 offset:7168
	v_mfma_scale_f32_16x16x128_f8f6f4 v[0:3], v[128:131], v[160:165], v[0:3], v208, v216 op_sel_hi:[0,0,0] cbsz:4 blgp:2
	s_cmp_eq_u32 s34, 13
	v_mfma_scale_f32_16x16x128_f8f6f4 v[4:7], v[128:131], v[166:171], v[4:7], v208, v217 op_sel_hi:[0,0,0] cbsz:4 blgp:2
	s_cselect_b32 s36, s38, s36
	v_mfma_scale_f32_16x16x128_f8f6f4 v[8:11], v[128:131], v[172:177], v[8:11], v208, v218 op_sel_hi:[0,0,0] cbsz:4 blgp:2
	s_cselect_b32 s37, s39, s37
	v_mfma_scale_f32_16x16x128_f8f6f4 v[12:15], v[128:131], v[178:183], v[12:15], v208, v219 op_sel_hi:[0,0,0] cbsz:4 blgp:2
	s_mov_b32 m0, s40
	v_mfma_scale_f32_16x16x128_f8f6f4 v[16:19], v[132:135], v[160:165], v[16:19], v209, v216 op_sel_hi:[0,0,0] cbsz:4 blgp:2
	ds_read_b128 v[184:187], v241 offset:0
	v_mfma_scale_f32_16x16x128_f8f6f4 v[20:23], v[132:135], v[166:171], v[20:23], v209, v217 op_sel_hi:[0,0,0] cbsz:4 blgp:2
	buffer_load_dwordx4 v221, s[4:7], s36 offen lds
	v_mfma_scale_f32_16x16x128_f8f6f4 v[24:27], v[132:135], v[172:177], v[24:27], v209, v218 op_sel_hi:[0,0,0] cbsz:4 blgp:2
	s_add_u32 m0, s40, 0x2000
	v_mfma_scale_f32_16x16x128_f8f6f4 v[28:31], v[132:135], v[178:183], v[28:31], v209, v219 op_sel_hi:[0,0,0] cbsz:4 blgp:2
	ds_read_b64 v[188:189], v242 offset:0
	v_mfma_scale_f32_16x16x128_f8f6f4 v[32:35], v[136:139], v[160:165], v[32:35], v210, v216 op_sel_hi:[0,0,0] cbsz:4 blgp:2
	buffer_load_dwordx4 v225, s[4:7], s36 offen lds
	v_mfma_scale_f32_16x16x128_f8f6f4 v[36:39], v[136:139], v[166:171], v[36:39], v210, v217 op_sel_hi:[0,0,0] cbsz:4 blgp:2
	s_add_u32 m0, s40, 0x4000
	v_mfma_scale_f32_16x16x128_f8f6f4 v[40:43], v[136:139], v[172:177], v[40:43], v210, v218 op_sel_hi:[0,0,0] cbsz:4 blgp:2
	ds_read_b128 v[190:193], v241 offset:1536
	v_mfma_scale_f32_16x16x128_f8f6f4 v[44:47], v[136:139], v[178:183], v[44:47], v210, v219 op_sel_hi:[0,0,0] cbsz:4 blgp:2
	buffer_load_dwordx4 v221, s[4:7], s37 offen lds
	v_mfma_scale_f32_16x16x128_f8f6f4 v[48:51], v[140:143], v[160:165], v[48:51], v211, v216 op_sel_hi:[0,0,0] cbsz:4 blgp:2
	s_add_u32 m0, s40, 0x6000
	v_mfma_scale_f32_16x16x128_f8f6f4 v[52:55], v[140:143], v[166:171], v[52:55], v211, v217 op_sel_hi:[0,0,0] cbsz:4 blgp:2
	ds_read_b64 v[194:195], v242 offset:1536
	v_mfma_scale_f32_16x16x128_f8f6f4 v[56:59], v[140:143], v[172:177], v[56:59], v211, v218 op_sel_hi:[0,0,0] cbsz:4 blgp:2
	buffer_load_dwordx4 v225, s[4:7], s37 offen lds
	v_mfma_scale_f32_16x16x128_f8f6f4 v[60:63], v[140:143], v[178:183], v[60:63], v211, v219 op_sel_hi:[0,0,0] cbsz:4 blgp:2
	s_add_u32 m0, s40, 0x8000
	v_mfma_scale_f32_16x16x128_f8f6f4 v[64:67], v[144:147], v[160:165], v[64:67], v212, v216 op_sel_hi:[0,0,0] cbsz:4 blgp:2
	ds_read_b128 v[196:199], v241 offset:3072
	v_mfma_scale_f32_16x16x128_f8f6f4 v[68:71], v[144:147], v[166:171], v[68:71], v212, v217 op_sel_hi:[0,0,0] cbsz:4 blgp:2
	buffer_load_dwordx4 v226, s[4:7], s37 offen lds
	v_mfma_scale_f32_16x16x128_f8f6f4 v[72:75], v[144:147], v[172:177], v[72:75], v212, v218 op_sel_hi:[0,0,0] cbsz:4 blgp:2
	ds_read_b64 v[200:201], v242 offset:3072
	v_mfma_scale_f32_16x16x128_f8f6f4 v[76:79], v[144:147], v[178:183], v[76:79], v212, v219 op_sel_hi:[0,0,0] cbsz:4 blgp:2
	ds_read_b128 v[202:205], v241 offset:4608
	v_mfma_scale_f32_16x16x128_f8f6f4 v[80:83], v[148:151], v[160:165], v[80:83], v213, v216 op_sel_hi:[0,0,0] cbsz:4 blgp:2
	ds_read_b64 v[206:207], v242 offset:4608
	v_mfma_scale_f32_16x16x128_f8f6f4 v[84:87], v[148:151], v[166:171], v[84:87], v213, v217 op_sel_hi:[0,0,0] cbsz:4 blgp:2
	s_add_u32 s36, s36, 0x4000
	v_mfma_scale_f32_16x16x128_f8f6f4 v[88:91], v[148:151], v[172:177], v[88:91], v213, v218 op_sel_hi:[0,0,0] cbsz:4 blgp:2
	s_add_u32 s37, s37, 0x6000
	v_mfma_scale_f32_16x16x128_f8f6f4 v[92:95], v[148:151], v[178:183], v[92:95], v213, v219 op_sel_hi:[0,0,0] cbsz:4 blgp:2
	s_add_u32 s40, s40, 0xa000
	v_mfma_scale_f32_16x16x128_f8f6f4 v[96:99], v[152:155], v[160:165], v[96:99], v214, v216 op_sel_hi:[0,0,0] cbsz:4 blgp:2
	s_sub_u32 s41, s40, 0x1e000
	v_mfma_scale_f32_16x16x128_f8f6f4 v[100:103], v[152:155], v[166:171], v[100:103], v214, v217 op_sel_hi:[0,0,0] cbsz:4 blgp:2
	s_cmp_ge_u32 s40, s49
	v_mfma_scale_f32_16x16x128_f8f6f4 v[104:107], v[152:155], v[172:177], v[104:107], v214, v218 op_sel_hi:[0,0,0] cbsz:4 blgp:2
	s_cselect_b32 s40, s41, s40
	v_mfma_scale_f32_16x16x128_f8f6f4 v[108:111], v[152:155], v[178:183], v[108:111], v214, v219 op_sel_hi:[0,0,0] cbsz:4 blgp:2
	ds_read_b128 v[128:131], v240 offset:0
	v_mfma_scale_f32_16x16x128_f8f6f4 v[112:115], v[156:159], v[160:165], v[112:115], v215, v216 op_sel_hi:[0,0,0] cbsz:4 blgp:2
	ds_read_b128 v[132:135], v240 offset:1024
	v_mfma_scale_f32_16x16x128_f8f6f4 v[116:119], v[156:159], v[166:171], v[116:119], v215, v217 op_sel_hi:[0,0,0] cbsz:4 blgp:2
	ds_read_b128 v[136:139], v240 offset:2048
	v_mfma_scale_f32_16x16x128_f8f6f4 v[120:123], v[156:159], v[172:177], v[120:123], v215, v218 op_sel_hi:[0,0,0] cbsz:4 blgp:2
	ds_read_b128 v[140:143], v240 offset:3072
	v_mfma_scale_f32_16x16x128_f8f6f4 v[124:127], v[156:159], v[178:183], v[124:127], v215, v219 op_sel_hi:[0,0,0] cbsz:4 blgp:2
	ds_read_b128 v[144:147], v240 offset:4096
	ds_read_b128 v[148:151], v240 offset:5120
	s_add_u32 s34, s34, 1
	s_waitcnt vmcnt(5)
	s_waitcnt lgkmcnt(0)
	s_barrier
	s_mul_i32 s35, s33, 0xa000
	v_add_u32_e32 v240, s35, v222
	v_add_u32_e32 v241, s35, v223
	v_add_u32_e32 v242, s35, v224
	s_add_u32 s33, s33, 1
	s_cmp_eq_u32 s33, 3
	s_cselect_b32 s33, 0, s33
	ds_read_b128 v[152:155], v240 offset:6144
	ds_read_b128 v[156:159], v240 offset:7168
	v_mfma_scale_f32_16x16x128_f8f6f4 v[0:3], v[128:131], v[184:189], v[0:3], v208, v216 op_sel_hi:[0,0,0] cbsz:4 blgp:2
	s_cmp_eq_u32 s34, 13
	v_mfma_scale_f32_16x16x128_f8f6f4 v[4:7], v[128:131], v[190:195], v[4:7], v208, v217 op_sel_hi:[0,0,0] cbsz:4 blgp:2
	s_cselect_b32 s36, s38, s36
	v_mfma_scale_f32_16x16x128_f8f6f4 v[8:11], v[128:131], v[196:201], v[8:11], v208, v218 op_sel_hi:[0,0,0] cbsz:4 blgp:2
	s_cselect_b32 s37, s39, s37
	v_mfma_scale_f32_16x16x128_f8f6f4 v[12:15], v[128:131], v[202:207], v[12:15], v208, v219 op_sel_hi:[0,0,0] cbsz:4 blgp:2
	s_mov_b32 m0, s40
	v_mfma_scale_f32_16x16x128_f8f6f4 v[16:19], v[132:135], v[184:189], v[16:19], v209, v216 op_sel_hi:[0,0,0] cbsz:4 blgp:2
	ds_read_b128 v[160:163], v241 offset:0
	v_mfma_scale_f32_16x16x128_f8f6f4 v[20:23], v[132:135], v[190:195], v[20:23], v209, v217 op_sel_hi:[0,0,0] cbsz:4 blgp:2
	buffer_load_dwordx4 v221, s[4:7], s36 offen lds
	v_mfma_scale_f32_16x16x128_f8f6f4 v[24:27], v[132:135], v[196:201], v[24:27], v209, v218 op_sel_hi:[0,0,0] cbsz:4 blgp:2
	s_add_u32 m0, s40, 0x2000
	v_mfma_scale_f32_16x16x128_f8f6f4 v[28:31], v[132:135], v[202:207], v[28:31], v209, v219 op_sel_hi:[0,0,0] cbsz:4 blgp:2
	ds_read_b64 v[164:165], v242 offset:0
	v_mfma_scale_f32_16x16x128_f8f6f4 v[32:35], v[136:139], v[184:189], v[32:35], v210, v216 op_sel_hi:[0,0,0] cbsz:4 blgp:2
	buffer_load_dwordx4 v225, s[4:7], s36 offen lds
	v_mfma_scale_f32_16x16x128_f8f6f4 v[36:39], v[136:139], v[190:195], v[36:39], v210, v217 op_sel_hi:[0,0,0] cbsz:4 blgp:2
	s_add_u32 m0, s40, 0x4000
	v_mfma_scale_f32_16x16x128_f8f6f4 v[40:43], v[136:139], v[196:201], v[40:43], v210, v218 op_sel_hi:[0,0,0] cbsz:4 blgp:2
	ds_read_b128 v[166:169], v241 offset:1536
	v_mfma_scale_f32_16x16x128_f8f6f4 v[44:47], v[136:139], v[202:207], v[44:47], v210, v219 op_sel_hi:[0,0,0] cbsz:4 blgp:2
	buffer_load_dwordx4 v221, s[4:7], s37 offen lds
	v_mfma_scale_f32_16x16x128_f8f6f4 v[48:51], v[140:143], v[184:189], v[48:51], v211, v216 op_sel_hi:[0,0,0] cbsz:4 blgp:2
	s_add_u32 m0, s40, 0x6000
	v_mfma_scale_f32_16x16x128_f8f6f4 v[52:55], v[140:143], v[190:195], v[52:55], v211, v217 op_sel_hi:[0,0,0] cbsz:4 blgp:2
	ds_read_b64 v[170:171], v242 offset:1536
	v_mfma_scale_f32_16x16x128_f8f6f4 v[56:59], v[140:143], v[196:201], v[56:59], v211, v218 op_sel_hi:[0,0,0] cbsz:4 blgp:2
	buffer_load_dwordx4 v225, s[4:7], s37 offen lds
	v_mfma_scale_f32_16x16x128_f8f6f4 v[60:63], v[140:143], v[202:207], v[60:63], v211, v219 op_sel_hi:[0,0,0] cbsz:4 blgp:2
	s_add_u32 m0, s40, 0x8000
	v_mfma_scale_f32_16x16x128_f8f6f4 v[64:67], v[144:147], v[184:189], v[64:67], v212, v216 op_sel_hi:[0,0,0] cbsz:4 blgp:2
	ds_read_b128 v[172:175], v241 offset:3072
	v_mfma_scale_f32_16x16x128_f8f6f4 v[68:71], v[144:147], v[190:195], v[68:71], v212, v217 op_sel_hi:[0,0,0] cbsz:4 blgp:2
	buffer_load_dwordx4 v226, s[4:7], s37 offen lds
	v_mfma_scale_f32_16x16x128_f8f6f4 v[72:75], v[144:147], v[196:201], v[72:75], v212, v218 op_sel_hi:[0,0,0] cbsz:4 blgp:2
	ds_read_b64 v[176:177], v242 offset:3072
	v_mfma_scale_f32_16x16x128_f8f6f4 v[76:79], v[144:147], v[202:207], v[76:79], v212, v219 op_sel_hi:[0,0,0] cbsz:4 blgp:2
	ds_read_b128 v[178:181], v241 offset:4608
	v_mfma_scale_f32_16x16x128_f8f6f4 v[80:83], v[148:151], v[184:189], v[80:83], v213, v216 op_sel_hi:[0,0,0] cbsz:4 blgp:2
	ds_read_b64 v[182:183], v242 offset:4608
	v_mfma_scale_f32_16x16x128_f8f6f4 v[84:87], v[148:151], v[190:195], v[84:87], v213, v217 op_sel_hi:[0,0,0] cbsz:4 blgp:2
	s_add_u32 s36, s36, 0x4000
	v_mfma_scale_f32_16x16x128_f8f6f4 v[88:91], v[148:151], v[196:201], v[88:91], v213, v218 op_sel_hi:[0,0,0] cbsz:4 blgp:2
	s_add_u32 s37, s37, 0x6000
	v_mfma_scale_f32_16x16x128_f8f6f4 v[92:95], v[148:151], v[202:207], v[92:95], v213, v219 op_sel_hi:[0,0,0] cbsz:4 blgp:2
	s_add_u32 s40, s40, 0xa000
	v_mfma_scale_f32_16x16x128_f8f6f4 v[96:99], v[244:247], v[184:189], v[96:99], v214, v216 op_sel_hi:[0,0,0] cbsz:4 blgp:2
	s_sub_u32 s41, s40, 0x1e000
	v_mfma_scale_f32_16x16x128_f8f6f4 v[100:103], v[244:247], v[190:195], v[100:103], v214, v217 op_sel_hi:[0,0,0] cbsz:4 blgp:2
	s_cmp_ge_u32 s40, s49
	v_mfma_scale_f32_16x16x128_f8f6f4 v[104:107], v[244:247], v[196:201], v[104:107], v214, v218 op_sel_hi:[0,0,0] cbsz:4 blgp:2
	s_cselect_b32 s40, s41, s40
	v_mfma_scale_f32_16x16x128_f8f6f4 v[108:111], v[244:247], v[202:207], v[108:111], v214, v219 op_sel_hi:[0,0,0] cbsz:4 blgp:2
	ds_read_b128 v[128:131], v240 offset:0
	v_mfma_scale_f32_16x16x128_f8f6f4 v[112:115], v[252:255], v[184:189], v[112:115], v215, v216 op_sel_hi:[0,0,0] cbsz:4 blgp:2
	ds_read_b128 v[132:135], v240 offset:1024
	v_mfma_scale_f32_16x16x128_f8f6f4 v[116:119], v[252:255], v[190:195], v[116:119], v215, v217 op_sel_hi:[0,0,0] cbsz:4 blgp:2
	ds_read_b128 v[136:139], v240 offset:2048
	v_mfma_scale_f32_16x16x128_f8f6f4 v[120:123], v[252:255], v[196:201], v[120:123], v215, v218 op_sel_hi:[0,0,0] cbsz:4 blgp:2
	ds_read_b128 v[140:143], v240 offset:3072
	v_mfma_scale_f32_16x16x128_f8f6f4 v[124:127], v[252:255], v[202:207], v[124:127], v215, v219 op_sel_hi:[0,0,0] cbsz:4 blgp:2
	ds_read_b128 v[144:147], v240 offset:4096
	ds_read_b128 v[148:151], v240 offset:5120
	s_cmp_eq_u32 s34, 13
	s_cbranch_scc0 .Lnosc_or0
	s_add_u32 s44, s23, 1
	s_and_b32 s44, s44, 1
	s_cmp_lt_u32 s18, 4
	s_cselect_b32 s80, s26, s27
	s_cselect_b32 s82, s8, s10
	s_cselect_b32 s83, s9, s11
	s_lshl_b32 s80, s80, 10
	s_and_b32 s84, s18, 3
	s_lshl_b32 s84, s84, 8
	s_add_u32 s80, s80, s84
	s_add_u32 s82, s82, s80
	s_addc_u32 s83, s83, 0
	s_lshl_b32 s84, s44, 11
	s_lshl_b32 s85, s18, 8
	s_add_u32 s84, s84, s85
	s_add_u32 s84, s84, 0x1e000
	s_mov_b32 m0, s84
	v_lshlrev_b32_e32 v236, 2, v220
	global_load_lds_dword v236, s[82:83]
.Lnosc_or0:
	s_add_u32 s34, s34, 1
	s_cmp_lt_u32 s34, 16
	s_cbranch_scc1 .Lkloop0
	s_add_u32 s44, s23, 1
	s_and_b32 s44, s44, 1
	s_lshl_b32 s80, s44, 11
	s_add_u32 s80, s80, 0x1e000
	s_lshl_b32 s82, s19, 9
	s_add_u32 s82, s82, s80
	s_lshl_b32 s83, s20, 8
	s_add_u32 s83, s83, s80
	s_add_u32 s83, s83, 0x400
	v_and_b32_e32 v234, 15, v220
	v_lshlrev_b32_e32 v234, 2, v234
	v_add_u32_e32 v235, s83, v234
	v_add_u32_e32 v234, s82, v234
	ds_read_b32 v208, v234 offset:0
	ds_read_b32 v209, v234 offset:64
	ds_read_b32 v210, v234 offset:128
	ds_read_b32 v211, v234 offset:192
	ds_read_b32 v212, v234 offset:256
	ds_read_b32 v213, v234 offset:320
	ds_read_b32 v214, v234 offset:384
	ds_read_b32 v215, v234 offset:448
	ds_read_b32 v216, v235 offset:0
	ds_read_b32 v217, v235 offset:64
	ds_read_b32 v218, v235 offset:128
	ds_read_b32 v219, v235 offset:192
	v_exp_f32_e32 v236, v0
	v_exp_f32_e32 v237, v1
	v_exp_f32_e32 v238, v2
	v_exp_f32_e32 v239, v3
	s_add_u32 s23, s23, 1
	v_exp_f32_e32 v240, v16
	v_exp_f32_e32 v241, v17
	v_exp_f32_e32 v242, v18
	v_exp_f32_e32 v243, v19
	s_mov_b32 s24, s26
	v_mov_b32_e32 v228, v236
	v_mov_b32_e32 v229, v237
	v_pk_add_f32 v[228:229], v[228:229], v[238:239]
	v_pk_add_f32 v[228:229], v[228:229], v[240:241]
	s_mov_b32 s25, s27
	v_pk_add_f32 v[228:229], v[228:229], v[242:243]
	v_exp_f32_e32 v236, v32
	v_exp_f32_e32 v237, v33
	v_exp_f32_e32 v238, v34
	s_mov_b32 s28, s30
	v_exp_f32_e32 v239, v35
	v_exp_f32_e32 v240, v48
	v_exp_f32_e32 v241, v49
	v_exp_f32_e32 v242, v50
	s_mov_b32 s29, s31
	v_exp_f32_e32 v243, v51
	v_pk_add_f32 v[228:229], v[228:229], v[236:237]
	v_pk_add_f32 v[228:229], v[228:229], v[238:239]
	v_pk_add_f32 v[228:229], v[228:229], v[240:241]
	s_add_u32 s45, s23, 1
	v_pk_add_f32 v[228:229], v[228:229], v[242:243]
	v_exp_f32_e32 v236, v64
	v_exp_f32_e32 v237, v65
	v_exp_f32_e32 v238, v66
	s_sub_u32 s46, s22, 1
	v_exp_f32_e32 v239, v67
	v_exp_f32_e32 v240, v80
	v_exp_f32_e32 v241, v81
	v_exp_f32_e32 v242, v82
	s_min_u32 s45, s45, s46
	v_exp_f32_e32 v243, v83
	v_pk_add_f32 v[228:229], v[228:229], v[236:237]
	v_pk_add_f32 v[228:229], v[228:229], v[238:239]
	v_pk_add_f32 v[228:229], v[228:229], v[240:241]
	s_lshl_b32 s45, s45, 5
	v_pk_add_f32 v[228:229], v[228:229], v[242:243]
	v_exp_f32_e32 v236, v96
	v_exp_f32_e32 v237, v97
	v_exp_f32_e32 v238, v98
	s_add_u32 s45, s45, s21
	v_exp_f32_e32 v239, v99
	v_exp_f32_e32 v240, v112
	v_exp_f32_e32 v241, v113
	v_exp_f32_e32 v242, v114
	s_lshr_b32 s80, s45, 5
	v_exp_f32_e32 v243, v115
	v_pk_add_f32 v[228:229], v[228:229], v[236:237]
	v_pk_add_f32 v[228:229], v[228:229], v[238:239]
	v_pk_add_f32 v[228:229], v[228:229], v[240:241]
	s_and_b32 s82, s45, 31
	v_pk_add_f32 v[228:229], v[228:229], v[242:243]
	v_exp_f32_e32 v236, v4
	v_exp_f32_e32 v237, v5
	v_exp_f32_e32 v238, v6
	s_lshr_b32 s83, s80, 1
	v_exp_f32_e32 v239, v7
	v_exp_f32_e32 v240, v20
	v_exp_f32_e32 v241, v21
	v_exp_f32_e32 v242, v22
	s_lshl_b32 s83, s83, 2
	v_exp_f32_e32 v243, v23
	v_mov_b32_e32 v230, v236
	v_mov_b32_e32 v231, v237
	v_pk_add_f32 v[230:231], v[230:231], v[238:239]
	s_lshr_b32 s84, s82, 3
	v_pk_add_f32 v[230:231], v[230:231], v[240:241]
	v_pk_add_f32 v[230:231], v[230:231], v[242:243]
	v_exp_f32_e32 v236, v36
	v_exp_f32_e32 v237, v37
	s_add_u32 s83, s83, s84
	v_exp_f32_e32 v238, v38
	v_exp_f32_e32 v239, v39
	v_exp_f32_e32 v240, v52
	v_exp_f32_e32 v241, v53
	s_and_b32 s84, s80, 1
	v_exp_f32_e32 v242, v54
	v_exp_f32_e32 v243, v55
	v_pk_add_f32 v[230:231], v[230:231], v[236:237]
	v_pk_add_f32 v[230:231], v[230:231], v[238:239]
	s_lshl_b32 s84, s84, 3
	v_pk_add_f32 v[230:231], v[230:231], v[240:241]
	v_pk_add_f32 v[230:231], v[230:231], v[242:243]
	v_exp_f32_e32 v236, v68
	v_exp_f32_e32 v237, v69
	s_and_b32 s85, s82, 7
	v_exp_f32_e32 v238, v70
	v_exp_f32_e32 v239, v71
	v_exp_f32_e32 v240, v84
	v_exp_f32_e32 v241, v85
	s_add_u32 s84, s84, s85
	v_exp_f32_e32 v242, v86
	v_exp_f32_e32 v243, v87
	v_pk_add_f32 v[230:231], v[230:231], v[236:237]
	v_pk_add_f32 v[230:231], v[230:231], v[238:239]
	s_sub_u32 s85, s45, 0x7c0
	v_pk_add_f32 v[230:231], v[230:231], v[240:241]
	v_pk_add_f32 v[230:231], v[230:231], v[242:243]
	v_exp_f32_e32 v236, v100
	v_exp_f32_e32 v237, v101
	s_cmpk_gt_u32 s45, 0x7bf
	v_exp_f32_e32 v238, v102
	v_exp_f32_e32 v239, v103
	v_exp_f32_e32 v240, v116
	v_exp_f32_e32 v241, v117
	s_cselect_b32 s26, 0x7c, s83
	v_exp_f32_e32 v242, v118
	v_exp_f32_e32 v243, v119
	v_pk_add_f32 v[230:231], v[230:231], v[236:237]
	v_pk_add_f32 v[230:231], v[230:231], v[238:239]
	s_cselect_b32 s27, s85, s84
	v_pk_add_f32 v[230:231], v[230:231], v[240:241]
	v_pk_add_f32 v[230:231], v[230:231], v[242:243]
	v_exp_f32_e32 v236, v8
	v_exp_f32_e32 v237, v9
	s_lshl_b32 s30, s26, 18
	v_exp_f32_e32 v238, v10
	v_exp_f32_e32 v239, v11
	v_exp_f32_e32 v240, v24
	v_exp_f32_e32 v241, v25
	s_mul_i32 s31, s27, 0x60000
	v_exp_f32_e32 v242, v26
	v_exp_f32_e32 v243, v27
	v_mov_b32_e32 v232, v236
	v_mov_b32_e32 v233, v237
	s_add_u32 s31, s31, 0x1f40000
	v_pk_add_f32 v[232:233], v[232:233], v[238:239]
	v_pk_add_f32 v[232:233], v[232:233], v[240:241]
	v_pk_add_f32 v[232:233], v[232:233], v[242:243]
	v_exp_f32_e32 v236, v40
	s_add_u32 s38, s30, s48
	v_exp_f32_e32 v237, v41
	v_exp_f32_e32 v238, v42
	v_exp_f32_e32 v239, v43
	v_exp_f32_e32 v240, v56
	s_add_u32 s39, s31, s48
	v_exp_f32_e32 v241, v57
	v_exp_f32_e32 v242, v58
	v_exp_f32_e32 v243, v59
	v_pk_add_f32 v[232:233], v[232:233], v[236:237]
	v_pk_add_f32 v[232:233], v[232:233], v[238:239]
	v_pk_add_f32 v[232:233], v[232:233], v[240:241]
	v_pk_add_f32 v[232:233], v[232:233], v[242:243]
	v_exp_f32_e32 v236, v72
	v_exp_f32_e32 v237, v73
	v_exp_f32_e32 v238, v74
	v_exp_f32_e32 v239, v75
	v_exp_f32_e32 v240, v88
	v_exp_f32_e32 v241, v89
	v_exp_f32_e32 v242, v90
	v_exp_f32_e32 v243, v91
	v_pk_add_f32 v[232:233], v[232:233], v[236:237]
	v_pk_add_f32 v[232:233], v[232:233], v[238:239]
	v_pk_add_f32 v[232:233], v[232:233], v[240:241]
	v_pk_add_f32 v[232:233], v[232:233], v[242:243]
	v_exp_f32_e32 v236, v104
	v_exp_f32_e32 v237, v105
	v_exp_f32_e32 v238, v106
	v_exp_f32_e32 v239, v107
	v_exp_f32_e32 v240, v120
	v_exp_f32_e32 v241, v121
	v_exp_f32_e32 v242, v122
	v_exp_f32_e32 v243, v123
	v_pk_add_f32 v[232:233], v[232:233], v[236:237]
	v_pk_add_f32 v[232:233], v[232:233], v[238:239]
	v_pk_add_f32 v[232:233], v[232:233], v[240:241]
	v_pk_add_f32 v[232:233], v[232:233], v[242:243]
	v_exp_f32_e32 v236, v12
	v_exp_f32_e32 v237, v13
	v_exp_f32_e32 v238, v14
	v_exp_f32_e32 v239, v15
	v_exp_f32_e32 v240, v28
	v_exp_f32_e32 v241, v29
	v_exp_f32_e32 v242, v30
	v_exp_f32_e32 v243, v31
	v_mov_b32_e32 v234, v236
	v_mov_b32_e32 v235, v237
	v_pk_add_f32 v[234:235], v[234:235], v[238:239]
	v_pk_add_f32 v[234:235], v[234:235], v[240:241]
	v_pk_add_f32 v[234:235], v[234:235], v[242:243]
	v_exp_f32_e32 v236, v44
	v_exp_f32_e32 v237, v45
	v_exp_f32_e32 v238, v46
	v_exp_f32_e32 v239, v47
	v_exp_f32_e32 v240, v60
	v_exp_f32_e32 v241, v61
	v_exp_f32_e32 v242, v62
	v_exp_f32_e32 v243, v63
	v_pk_add_f32 v[234:235], v[234:235], v[236:237]
	v_pk_add_f32 v[234:235], v[234:235], v[238:239]
	v_pk_add_f32 v[234:235], v[234:235], v[240:241]
	v_pk_add_f32 v[234:235], v[234:235], v[242:243]
	v_exp_f32_e32 v236, v76
	v_exp_f32_e32 v237, v77
	v_exp_f32_e32 v238, v78
	v_exp_f32_e32 v239, v79
	v_exp_f32_e32 v240, v92
	v_exp_f32_e32 v241, v93
	v_exp_f32_e32 v242, v94
	v_exp_f32_e32 v243, v95
	v_pk_add_f32 v[234:235], v[234:235], v[236:237]
	v_pk_add_f32 v[234:235], v[234:235], v[238:239]
	v_pk_add_f32 v[234:235], v[234:235], v[240:241]
	v_pk_add_f32 v[234:235], v[234:235], v[242:243]
	v_exp_f32_e32 v236, v108
	v_exp_f32_e32 v237, v109
	v_exp_f32_e32 v238, v110
	v_exp_f32_e32 v239, v111
	v_exp_f32_e32 v240, v124
	v_exp_f32_e32 v241, v125
	v_exp_f32_e32 v242, v126
	v_exp_f32_e32 v243, v127
	v_pk_add_f32 v[234:235], v[234:235], v[236:237]
	v_pk_add_f32 v[234:235], v[234:235], v[238:239]
	v_pk_add_f32 v[234:235], v[234:235], v[240:241]
	v_pk_add_f32 v[234:235], v[234:235], v[242:243]
	v_add_f32_e32 v228, v228, v229
	v_add_f32_e32 v230, v230, v231
	v_add_f32_e32 v232, v232, v233
	v_add_f32_e32 v234, v234, v235
	s_nop 1
	v_permlane16_swap_b32_e32 v228, v230
	v_permlane16_swap_b32_e32 v232, v234
	s_nop 1
	v_add_f32_e32 v228, v228, v230
	v_add_f32_e32 v232, v232, v234
	s_nop 1
	v_permlane32_swap_b32_e32 v228, v232
	s_nop 1
	v_add_f32_e32 v238, v228, v232
	v_cmp_nle_f32_e64 s[60:61], s56, v238
	v_cmp_nge_f32_e64 s[58:59], s57, v238
	s_nop 3
	s_or_b64 s[58:59], s[58:59], s[60:61]
	s_cmp_lg_u64 s[58:59], 0
	s_cbranch_scc1 .Lslow0
	global_atomic_add_f32 v[248:249], v238, off
	s_branch .Lepi_done0

.Ltile1:
	s_mov_b32 s34, 0
	s_waitcnt vmcnt(5)
	s_waitcnt lgkmcnt(0)
	s_barrier
	s_mul_i32 s35, s33, 0xa000
	v_add_u32_e32 v240, s35, v222
	v_add_u32_e32 v241, s35, v223
	v_add_u32_e32 v242, s35, v224
	s_add_u32 s33, s33, 1
	s_cmp_eq_u32 s33, 3
	s_cselect_b32 s33, 0, s33
	ds_read_b128 v[244:247], v240 offset:6144
	ds_read_b128 v[252:255], v240 offset:7168
	v_mfma_scale_f32_16x16x128_f8f6f4 v[0:3], v[128:131], v[160:165], 0, v208, v216 op_sel_hi:[0,0,0] cbsz:4 blgp:2
	v_mfma_scale_f32_16x16x128_f8f6f4 v[4:7], v[128:131], v[166:171], 0, v208, v217 op_sel_hi:[0,0,0] cbsz:4 blgp:2
	v_mfma_scale_f32_16x16x128_f8f6f4 v[8:11], v[128:131], v[172:177], 0, v208, v218 op_sel_hi:[0,0,0] cbsz:4 blgp:2
	s_cmp_eq_u32 s34, 13
	v_mfma_scale_f32_16x16x128_f8f6f4 v[12:15], v[128:131], v[178:183], 0, v208, v219 op_sel_hi:[0,0,0] cbsz:4 blgp:2
	s_cselect_b32 s36, s38, s36
	v_mfma_scale_f32_16x16x128_f8f6f4 v[16:19], v[132:135], v[160:165], 0, v209, v216 op_sel_hi:[0,0,0] cbsz:4 blgp:2
	s_cselect_b32 s37, s39, s37
	v_mfma_scale_f32_16x16x128_f8f6f4 v[20:23], v[132:135], v[166:171], 0, v209, v217 op_sel_hi:[0,0,0] cbsz:4 blgp:2
	s_mov_b32 m0, s40
	v_mfma_scale_f32_16x16x128_f8f6f4 v[24:27], v[132:135], v[172:177], 0, v209, v218 op_sel_hi:[0,0,0] cbsz:4 blgp:2
	ds_read_b128 v[184:187], v241 offset:0
	v_mfma_scale_f32_16x16x128_f8f6f4 v[28:31], v[132:135], v[178:183], 0, v209, v219 op_sel_hi:[0,0,0] cbsz:4 blgp:2
	buffer_load_dwordx4 v221, s[4:7], s36 offen lds
	v_mfma_scale_f32_16x16x128_f8f6f4 v[32:35], v[136:139], v[160:165], 0, v210, v216 op_sel_hi:[0,0,0] cbsz:4 blgp:2
	s_add_u32 m0, s40, 0x2000
	v_mfma_scale_f32_16x16x128_f8f6f4 v[36:39], v[136:139], v[166:171], 0, v210, v217 op_sel_hi:[0,0,0] cbsz:4 blgp:2
	ds_read_b64 v[188:189], v242 offset:0
	v_mfma_scale_f32_16x16x128_f8f6f4 v[40:43], v[136:139], v[172:177], 0, v210, v218 op_sel_hi:[0,0,0] cbsz:4 blgp:2
	buffer_load_dwordx4 v225, s[4:7], s36 offen lds
	v_mfma_scale_f32_16x16x128_f8f6f4 v[44:47], v[136:139], v[178:183], 0, v210, v219 op_sel_hi:[0,0,0] cbsz:4 blgp:2
	s_add_u32 m0, s40, 0x4000
	v_mfma_scale_f32_16x16x128_f8f6f4 v[48:51], v[140:143], v[160:165], 0, v211, v216 op_sel_hi:[0,0,0] cbsz:4 blgp:2
	ds_read_b128 v[190:193], v241 offset:1536
	v_mfma_scale_f32_16x16x128_f8f6f4 v[52:55], v[140:143], v[166:171], 0, v211, v217 op_sel_hi:[0,0,0] cbsz:4 blgp:2
	buffer_load_dwordx4 v221, s[4:7], s37 offen lds
	v_mfma_scale_f32_16x16x128_f8f6f4 v[56:59], v[140:143], v[172:177], 0, v211, v218 op_sel_hi:[0,0,0] cbsz:4 blgp:2
	s_add_u32 m0, s40, 0x6000
	v_mfma_scale_f32_16x16x128_f8f6f4 v[60:63], v[140:143], v[178:183], 0, v211, v219 op_sel_hi:[0,0,0] cbsz:4 blgp:2
	ds_read_b64 v[194:195], v242 offset:1536
	v_mfma_scale_f32_16x16x128_f8f6f4 v[64:67], v[144:147], v[160:165], 0, v212, v216 op_sel_hi:[0,0,0] cbsz:4 blgp:2
	buffer_load_dwordx4 v225, s[4:7], s37 offen lds
	v_mfma_scale_f32_16x16x128_f8f6f4 v[68:71], v[144:147], v[166:171], 0, v212, v217 op_sel_hi:[0,0,0] cbsz:4 blgp:2
	s_add_u32 m0, s40, 0x8000
	v_mfma_scale_f32_16x16x128_f8f6f4 v[72:75], v[144:147], v[172:177], 0, v212, v218 op_sel_hi:[0,0,0] cbsz:4 blgp:2
	ds_read_b128 v[196:199], v241 offset:3072
	v_mfma_scale_f32_16x16x128_f8f6f4 v[76:79], v[144:147], v[178:183], 0, v212, v219 op_sel_hi:[0,0,0] cbsz:4 blgp:2
	buffer_load_dwordx4 v226, s[4:7], s37 offen lds
	v_mfma_scale_f32_16x16x128_f8f6f4 v[80:83], v[148:151], v[160:165], 0, v213, v216 op_sel_hi:[0,0,0] cbsz:4 blgp:2
	ds_read_b64 v[200:201], v242 offset:3072
	v_mfma_scale_f32_16x16x128_f8f6f4 v[84:87], v[148:151], v[166:171], 0, v213, v217 op_sel_hi:[0,0,0] cbsz:4 blgp:2
	ds_read_b128 v[202:205], v241 offset:4608
	v_mfma_scale_f32_16x16x128_f8f6f4 v[88:91], v[148:151], v[172:177], 0, v213, v218 op_sel_hi:[0,0,0] cbsz:4 blgp:2
	ds_read_b64 v[206:207], v242 offset:4608
	v_mfma_scale_f32_16x16x128_f8f6f4 v[92:95], v[148:151], v[178:183], 0, v213, v219 op_sel_hi:[0,0,0] cbsz:4 blgp:2
	s_add_u32 s36, s36, 0x4000
	v_mfma_scale_f32_16x16x128_f8f6f4 v[96:99], v[152:155], v[160:165], 0, v214, v216 op_sel_hi:[0,0,0] cbsz:4 blgp:2
	s_add_u32 s37, s37, 0x6000
	v_mfma_scale_f32_16x16x128_f8f6f4 v[100:103], v[152:155], v[166:171], 0, v214, v217 op_sel_hi:[0,0,0] cbsz:4 blgp:2
	s_add_u32 s40, s40, 0xa000
	v_mfma_scale_f32_16x16x128_f8f6f4 v[104:107], v[152:155], v[172:177], 0, v214, v218 op_sel_hi:[0,0,0] cbsz:4 blgp:2
	s_sub_u32 s41, s40, 0x1e000
	v_mfma_scale_f32_16x16x128_f8f6f4 v[108:111], v[152:155], v[178:183], 0, v214, v219 op_sel_hi:[0,0,0] cbsz:4 blgp:2
	s_cmp_ge_u32 s40, s49
	v_mfma_scale_f32_16x16x128_f8f6f4 v[112:115], v[156:159], v[160:165], 0, v215, v216 op_sel_hi:[0,0,0] cbsz:4 blgp:2
	s_cselect_b32 s40, s41, s40
	v_mfma_scale_f32_16x16x128_f8f6f4 v[116:119], v[156:159], v[166:171], 0, v215, v217 op_sel_hi:[0,0,0] cbsz:4 blgp:2
	ds_read_b128 v[128:131], v240 offset:0
	v_mfma_scale_f32_16x16x128_f8f6f4 v[120:123], v[156:159], v[172:177], 0, v215, v218 op_sel_hi:[0,0,0] cbsz:4 blgp:2
	ds_read_b128 v[132:135], v240 offset:1024
	v_mfma_scale_f32_16x16x128_f8f6f4 v[124:127], v[156:159], v[178:183], 0, v215, v219 op_sel_hi:[0,0,0] cbsz:4 blgp:2
	ds_read_b128 v[136:139], v240 offset:2048
	ds_read_b128 v[140:143], v240 offset:3072
	ds_read_b128 v[144:147], v240 offset:4096
	ds_read_b128 v[148:151], v240 offset:5120
	s_add_u32 s34, s34, 1
	s_waitcnt vmcnt(5)
	s_waitcnt lgkmcnt(0)
	s_barrier
	s_mul_i32 s35, s33, 0xa000
	v_add_u32_e32 v240, s35, v222
	v_add_u32_e32 v241, s35, v223
	v_add_u32_e32 v242, s35, v224
	s_add_u32 s33, s33, 1
	s_cmp_eq_u32 s33, 3
	s_cselect_b32 s33, 0, s33
	ds_read_b128 v[152:155], v240 offset:6144
	ds_read_b128 v[156:159], v240 offset:7168
	v_mfma_scale_f32_16x16x128_f8f6f4 v[0:3], v[128:131], v[184:189], v[0:3], v208, v216 op_sel_hi:[0,0,0] cbsz:4 blgp:2
	v_mfma_scale_f32_16x16x128_f8f6f4 v[4:7], v[128:131], v[190:195], v[4:7], v208, v217 op_sel_hi:[0,0,0] cbsz:4 blgp:2
	v_mfma_scale_f32_16x16x128_f8f6f4 v[8:11], v[128:131], v[196:201], v[8:11], v208, v218 op_sel_hi:[0,0,0] cbsz:4 blgp:2
	s_cmp_eq_u32 s34, 13
	v_mfma_scale_f32_16x16x128_f8f6f4 v[12:15], v[128:131], v[202:207], v[12:15], v208, v219 op_sel_hi:[0,0,0] cbsz:4 blgp:2
	s_cselect_b32 s36, s38, s36
	v_mfma_scale_f32_16x16x128_f8f6f4 v[16:19], v[132:135], v[184:189], v[16:19], v209, v216 op_sel_hi:[0,0,0] cbsz:4 blgp:2
	s_cselect_b32 s37, s39, s37
	v_mfma_scale_f32_16x16x128_f8f6f4 v[20:23], v[132:135], v[190:195], v[20:23], v209, v217 op_sel_hi:[0,0,0] cbsz:4 blgp:2
	s_mov_b32 m0, s40
	v_mfma_scale_f32_16x16x128_f8f6f4 v[24:27], v[132:135], v[196:201], v[24:27], v209, v218 op_sel_hi:[0,0,0] cbsz:4 blgp:2
	ds_read_b128 v[160:163], v241 offset:0
	v_mfma_scale_f32_16x16x128_f8f6f4 v[28:31], v[132:135], v[202:207], v[28:31], v209, v219 op_sel_hi:[0,0,0] cbsz:4 blgp:2
	buffer_load_dwordx4 v221, s[4:7], s36 offen lds
	v_mfma_scale_f32_16x16x128_f8f6f4 v[32:35], v[136:139], v[184:189], v[32:35], v210, v216 op_sel_hi:[0,0,0] cbsz:4 blgp:2
	s_add_u32 m0, s40, 0x2000
	v_mfma_scale_f32_16x16x128_f8f6f4 v[36:39], v[136:139], v[190:195], v[36:39], v210, v217 op_sel_hi:[0,0,0] cbsz:4 blgp:2
	ds_read_b64 v[164:165], v242 offset:0
	v_mfma_scale_f32_16x16x128_f8f6f4 v[40:43], v[136:139], v[196:201], v[40:43], v210, v218 op_sel_hi:[0,0,0] cbsz:4 blgp:2
	buffer_load_dwordx4 v225, s[4:7], s36 offen lds
	v_mfma_scale_f32_16x16x128_f8f6f4 v[44:47], v[136:139], v[202:207], v[44:47], v210, v219 op_sel_hi:[0,0,0] cbsz:4 blgp:2
	s_add_u32 m0, s40, 0x4000
	v_mfma_scale_f32_16x16x128_f8f6f4 v[48:51], v[140:143], v[184:189], v[48:51], v211, v216 op_sel_hi:[0,0,0] cbsz:4 blgp:2
	ds_read_b128 v[166:169], v241 offset:1536
	v_mfma_scale_f32_16x16x128_f8f6f4 v[52:55], v[140:143], v[190:195], v[52:55], v211, v217 op_sel_hi:[0,0,0] cbsz:4 blgp:2
	buffer_load_dwordx4 v221, s[4:7], s37 offen lds
	v_mfma_scale_f32_16x16x128_f8f6f4 v[56:59], v[140:143], v[196:201], v[56:59], v211, v218 op_sel_hi:[0,0,0] cbsz:4 blgp:2
	s_add_u32 m0, s40, 0x6000
	v_mfma_scale_f32_16x16x128_f8f6f4 v[60:63], v[140:143], v[202:207], v[60:63], v211, v219 op_sel_hi:[0,0,0] cbsz:4 blgp:2
	ds_read_b64 v[170:171], v242 offset:1536
	v_mfma_scale_f32_16x16x128_f8f6f4 v[64:67], v[144:147], v[184:189], v[64:67], v212, v216 op_sel_hi:[0,0,0] cbsz:4 blgp:2
	buffer_load_dwordx4 v225, s[4:7], s37 offen lds
	v_mfma_scale_f32_16x16x128_f8f6f4 v[68:71], v[144:147], v[190:195], v[68:71], v212, v217 op_sel_hi:[0,0,0] cbsz:4 blgp:2
	s_add_u32 m0, s40, 0x8000
	v_mfma_scale_f32_16x16x128_f8f6f4 v[72:75], v[144:147], v[196:201], v[72:75], v212, v218 op_sel_hi:[0,0,0] cbsz:4 blgp:2
	ds_read_b128 v[172:175], v241 offset:3072
	v_mfma_scale_f32_16x16x128_f8f6f4 v[76:79], v[144:147], v[202:207], v[76:79], v212, v219 op_sel_hi:[0,0,0] cbsz:4 blgp:2
	buffer_load_dwordx4 v226, s[4:7], s37 offen lds
	v_mfma_scale_f32_16x16x128_f8f6f4 v[80:83], v[148:151], v[184:189], v[80:83], v213, v216 op_sel_hi:[0,0,0] cbsz:4 blgp:2
	ds_read_b64 v[176:177], v242 offset:3072
	v_mfma_scale_f32_16x16x128_f8f6f4 v[84:87], v[148:151], v[190:195], v[84:87], v213, v217 op_sel_hi:[0,0,0] cbsz:4 blgp:2
	ds_read_b128 v[178:181], v241 offset:4608
	v_mfma_scale_f32_16x16x128_f8f6f4 v[88:91], v[148:151], v[196:201], v[88:91], v213, v218 op_sel_hi:[0,0,0] cbsz:4 blgp:2
	ds_read_b64 v[182:183], v242 offset:4608
	v_mfma_scale_f32_16x16x128_f8f6f4 v[92:95], v[148:151], v[202:207], v[92:95], v213, v219 op_sel_hi:[0,0,0] cbsz:4 blgp:2
	s_add_u32 s36, s36, 0x4000
	v_mfma_scale_f32_16x16x128_f8f6f4 v[96:99], v[244:247], v[184:189], v[96:99], v214, v216 op_sel_hi:[0,0,0] cbsz:4 blgp:2
	s_add_u32 s37, s37, 0x6000
	v_mfma_scale_f32_16x16x128_f8f6f4 v[100:103], v[244:247], v[190:195], v[100:103], v214, v217 op_sel_hi:[0,0,0] cbsz:4 blgp:2
	s_add_u32 s40, s40, 0xa000
	v_mfma_scale_f32_16x16x128_f8f6f4 v[104:107], v[244:247], v[196:201], v[104:107], v214, v218 op_sel_hi:[0,0,0] cbsz:4 blgp:2
	s_sub_u32 s41, s40, 0x1e000
	v_mfma_scale_f32_16x16x128_f8f6f4 v[108:111], v[244:247], v[202:207], v[108:111], v214, v219 op_sel_hi:[0,0,0] cbsz:4 blgp:2
	s_cmp_ge_u32 s40, s49
	v_mfma_scale_f32_16x16x128_f8f6f4 v[112:115], v[252:255], v[184:189], v[112:115], v215, v216 op_sel_hi:[0,0,0] cbsz:4 blgp:2
	s_cselect_b32 s40, s41, s40
	v_mfma_scale_f32_16x16x128_f8f6f4 v[116:119], v[252:255], v[190:195], v[116:119], v215, v217 op_sel_hi:[0,0,0] cbsz:4 blgp:2
	ds_read_b128 v[128:131], v240 offset:0
	v_mfma_scale_f32_16x16x128_f8f6f4 v[120:123], v[252:255], v[196:201], v[120:123], v215, v218 op_sel_hi:[0,0,0] cbsz:4 blgp:2
	ds_read_b128 v[132:135], v240 offset:1024
	v_mfma_scale_f32_16x16x128_f8f6f4 v[124:127], v[252:255], v[202:207], v[124:127], v215, v219 op_sel_hi:[0,0,0] cbsz:4 blgp:2
	ds_read_b128 v[136:139], v240 offset:2048
	ds_read_b128 v[140:143], v240 offset:3072
	ds_read_b128 v[144:147], v240 offset:4096
	ds_read_b128 v[148:151], v240 offset:5120
	s_add_u32 s34, s34, 1
.Lkloop1:
	s_waitcnt vmcnt(5)
	s_waitcnt lgkmcnt(0)
	s_barrier
	s_mul_i32 s35, s33, 0xa000
	v_add_u32_e32 v240, s35, v222
	v_add_u32_e32 v241, s35, v223
	v_add_u32_e32 v242, s35, v224
	s_add_u32 s33, s33, 1
	s_cmp_eq_u32 s33, 3
	s_cselect_b32 s33, 0, s33
	ds_read_b128 v[244:247], v240 offset:6144
	ds_read_b128 v[252:255], v240 offset:7168
	v_mfma_scale_f32_16x16x128_f8f6f4 v[0:3], v[128:131], v[160:165], v[0:3], v208, v216 op_sel_hi:[0,0,0] cbsz:4 blgp:2
	v_mfma_scale_f32_16x16x128_f8f6f4 v[4:7], v[128:131], v[166:171], v[4:7], v208, v217 op_sel_hi:[0,0,0] cbsz:4 blgp:2
	v_mfma_scale_f32_16x16x128_f8f6f4 v[8:11], v[128:131], v[172:177], v[8:11], v208, v218 op_sel_hi:[0,0,0] cbsz:4 blgp:2
	s_cmp_eq_u32 s34, 13
	v_mfma_scale_f32_16x16x128_f8f6f4 v[12:15], v[128:131], v[178:183], v[12:15], v208, v219 op_sel_hi:[0,0,0] cbsz:4 blgp:2
	s_cselect_b32 s36, s38, s36
	v_mfma_scale_f32_16x16x128_f8f6f4 v[16:19], v[132:135], v[160:165], v[16:19], v209, v216 op_sel_hi:[0,0,0] cbsz:4 blgp:2
	s_cselect_b32 s37, s39, s37
	v_mfma_scale_f32_16x16x128_f8f6f4 v[20:23], v[132:135], v[166:171], v[20:23], v209, v217 op_sel_hi:[0,0,0] cbsz:4 blgp:2
	s_mov_b32 m0, s40
	v_mfma_scale_f32_16x16x128_f8f6f4 v[24:27], v[132:135], v[172:177], v[24:27], v209, v218 op_sel_hi:[0,0,0] cbsz:4 blgp:2
	ds_read_b128 v[184:187], v241 offset:0
	v_mfma_scale_f32_16x16x128_f8f6f4 v[28:31], v[132:135], v[178:183], v[28:31], v209, v219 op_sel_hi:[0,0,0] cbsz:4 blgp:2
	buffer_load_dwordx4 v221, s[4:7], s36 offen lds
	v_mfma_scale_f32_16x16x128_f8f6f4 v[32:35], v[136:139], v[160:165], v[32:35], v210, v216 op_sel_hi:[0,0,0] cbsz:4 blgp:2
	s_add_u32 m0, s40, 0x2000
	v_mfma_scale_f32_16x16x128_f8f6f4 v[36:39], v[136:139], v[166:171], v[36:39], v210, v217 op_sel_hi:[0,0,0] cbsz:4 blgp:2
	ds_read_b64 v[188:189], v242 offset:0
	v_mfma_scale_f32_16x16x128_f8f6f4 v[40:43], v[136:139], v[172:177], v[40:43], v210, v218 op_sel_hi:[0,0,0] cbsz:4 blgp:2
	buffer_load_dwordx4 v225, s[4:7], s36 offen lds
	v_mfma_scale_f32_16x16x128_f8f6f4 v[44:47], v[136:139], v[178:183], v[44:47], v210, v219 op_sel_hi:[0,0,0] cbsz:4 blgp:2
	s_add_u32 m0, s40, 0x4000
	v_mfma_scale_f32_16x16x128_f8f6f4 v[48:51], v[140:143], v[160:165], v[48:51], v211, v216 op_sel_hi:[0,0,0] cbsz:4 blgp:2
	ds_read_b128 v[190:193], v241 offset:1536
	v_mfma_scale_f32_16x16x128_f8f6f4 v[52:55], v[140:143], v[166:171], v[52:55], v211, v217 op_sel_hi:[0,0,0] cbsz:4 blgp:2
	buffer_load_dwordx4 v221, s[4:7], s37 offen lds
	v_mfma_scale_f32_16x16x128_f8f6f4 v[56:59], v[140:143], v[172:177], v[56:59], v211, v218 op_sel_hi:[0,0,0] cbsz:4 blgp:2
	s_add_u32 m0, s40, 0x6000
	v_mfma_scale_f32_16x16x128_f8f6f4 v[60:63], v[140:143], v[178:183], v[60:63], v211, v219 op_sel_hi:[0,0,0] cbsz:4 blgp:2
	ds_read_b64 v[194:195], v242 offset:1536
	v_mfma_scale_f32_16x16x128_f8f6f4 v[64:67], v[144:147], v[160:165], v[64:67], v212, v216 op_sel_hi:[0,0,0] cbsz:4 blgp:2
	buffer_load_dwordx4 v225, s[4:7], s37 offen lds
	v_mfma_scale_f32_16x16x128_f8f6f4 v[68:71], v[144:147], v[166:171], v[68:71], v212, v217 op_sel_hi:[0,0,0] cbsz:4 blgp:2
	s_add_u32 m0, s40, 0x8000
	v_mfma_scale_f32_16x16x128_f8f6f4 v[72:75], v[144:147], v[172:177], v[72:75], v212, v218 op_sel_hi:[0,0,0] cbsz:4 blgp:2
	ds_read_b128 v[196:199], v241 offset:3072
	v_mfma_scale_f32_16x16x128_f8f6f4 v[76:79], v[144:147], v[178:183], v[76:79], v212, v219 op_sel_hi:[0,0,0] cbsz:4 blgp:2
	buffer_load_dwordx4 v226, s[4:7], s37 offen lds
	v_mfma_scale_f32_16x16x128_f8f6f4 v[80:83], v[148:151], v[160:165], v[80:83], v213, v216 op_sel_hi:[0,0,0] cbsz:4 blgp:2
	ds_read_b64 v[200:201], v242 offset:3072
	v_mfma_scale_f32_16x16x128_f8f6f4 v[84:87], v[148:151], v[166:171], v[84:87], v213, v217 op_sel_hi:[0,0,0] cbsz:4 blgp:2
	ds_read_b128 v[202:205], v241 offset:4608
	v_mfma_scale_f32_16x16x128_f8f6f4 v[88:91], v[148:151], v[172:177], v[88:91], v213, v218 op_sel_hi:[0,0,0] cbsz:4 blgp:2
	ds_read_b64 v[206:207], v242 offset:4608
	v_mfma_scale_f32_16x16x128_f8f6f4 v[92:95], v[148:151], v[178:183], v[92:95], v213, v219 op_sel_hi:[0,0,0] cbsz:4 blgp:2
	s_add_u32 s36, s36, 0x4000
	v_mfma_scale_f32_16x16x128_f8f6f4 v[96:99], v[152:155], v[160:165], v[96:99], v214, v216 op_sel_hi:[0,0,0] cbsz:4 blgp:2
	s_add_u32 s37, s37, 0x6000
	v_mfma_scale_f32_16x16x128_f8f6f4 v[100:103], v[152:155], v[166:171], v[100:103], v214, v217 op_sel_hi:[0,0,0] cbsz:4 blgp:2
	s_add_u32 s40, s40, 0xa000
	v_mfma_scale_f32_16x16x128_f8f6f4 v[104:107], v[152:155], v[172:177], v[104:107], v214, v218 op_sel_hi:[0,0,0] cbsz:4 blgp:2
	s_sub_u32 s41, s40, 0x1e000
	v_mfma_scale_f32_16x16x128_f8f6f4 v[108:111], v[152:155], v[178:183], v[108:111], v214, v219 op_sel_hi:[0,0,0] cbsz:4 blgp:2
	s_cmp_ge_u32 s40, s49
	v_mfma_scale_f32_16x16x128_f8f6f4 v[112:115], v[156:159], v[160:165], v[112:115], v215, v216 op_sel_hi:[0,0,0] cbsz:4 blgp:2
	s_cselect_b32 s40, s41, s40
	v_mfma_scale_f32_16x16x128_f8f6f4 v[116:119], v[156:159], v[166:171], v[116:119], v215, v217 op_sel_hi:[0,0,0] cbsz:4 blgp:2
	ds_read_b128 v[128:131], v240 offset:0
	v_mfma_scale_f32_16x16x128_f8f6f4 v[120:123], v[156:159], v[172:177], v[120:123], v215, v218 op_sel_hi:[0,0,0] cbsz:4 blgp:2
	ds_read_b128 v[132:135], v240 offset:1024
	v_mfma_scale_f32_16x16x128_f8f6f4 v[124:127], v[156:159], v[178:183], v[124:127], v215, v219 op_sel_hi:[0,0,0] cbsz:4 blgp:2
	ds_read_b128 v[136:139], v240 offset:2048
	ds_read_b128 v[140:143], v240 offset:3072
	ds_read_b128 v[144:147], v240 offset:4096
	ds_read_b128 v[148:151], v240 offset:5120
	s_add_u32 s34, s34, 1
	s_waitcnt vmcnt(5)
	s_waitcnt lgkmcnt(0)
	s_barrier
	s_mul_i32 s35, s33, 0xa000
	v_add_u32_e32 v240, s35, v222
	v_add_u32_e32 v241, s35, v223
	v_add_u32_e32 v242, s35, v224
	s_add_u32 s33, s33, 1
	s_cmp_eq_u32 s33, 3
	s_cselect_b32 s33, 0, s33
	ds_read_b128 v[152:155], v240 offset:6144
	ds_read_b128 v[156:159], v240 offset:7168
	v_mfma_scale_f32_16x16x128_f8f6f4 v[0:3], v[128:131], v[184:189], v[0:3], v208, v216 op_sel_hi:[0,0,0] cbsz:4 blgp:2
	v_mfma_scale_f32_16x16x128_f8f6f4 v[4:7], v[128:131], v[190:195], v[4:7], v208, v217 op_sel_hi:[0,0,0] cbsz:4 blgp:2
	v_mfma_scale_f32_16x16x128_f8f6f4 v[8:11], v[128:131], v[196:201], v[8:11], v208, v218 op_sel_hi:[0,0,0] cbsz:4 blgp:2
	s_cmp_eq_u32 s34, 13
	v_mfma_scale_f32_16x16x128_f8f6f4 v[12:15], v[128:131], v[202:207], v[12:15], v208, v219 op_sel_hi:[0,0,0] cbsz:4 blgp:2
	s_cselect_b32 s36, s38, s36
	v_mfma_scale_f32_16x16x128_f8f6f4 v[16:19], v[132:135], v[184:189], v[16:19], v209, v216 op_sel_hi:[0,0,0] cbsz:4 blgp:2
	s_cselect_b32 s37, s39, s37
	v_mfma_scale_f32_16x16x128_f8f6f4 v[20:23], v[132:135], v[190:195], v[20:23], v209, v217 op_sel_hi:[0,0,0] cbsz:4 blgp:2
	s_mov_b32 m0, s40
	v_mfma_scale_f32_16x16x128_f8f6f4 v[24:27], v[132:135], v[196:201], v[24:27], v209, v218 op_sel_hi:[0,0,0] cbsz:4 blgp:2
	ds_read_b128 v[160:163], v241 offset:0
	v_mfma_scale_f32_16x16x128_f8f6f4 v[28:31], v[132:135], v[202:207], v[28:31], v209, v219 op_sel_hi:[0,0,0] cbsz:4 blgp:2
	buffer_load_dwordx4 v221, s[4:7], s36 offen lds
	v_mfma_scale_f32_16x16x128_f8f6f4 v[32:35], v[136:139], v[184:189], v[32:35], v210, v216 op_sel_hi:[0,0,0] cbsz:4 blgp:2
	s_add_u32 m0, s40, 0x2000
	v_mfma_scale_f32_16x16x128_f8f6f4 v[36:39], v[136:139], v[190:195], v[36:39], v210, v217 op_sel_hi:[0,0,0] cbsz:4 blgp:2
	ds_read_b64 v[164:165], v242 offset:0
	v_mfma_scale_f32_16x16x128_f8f6f4 v[40:43], v[136:139], v[196:201], v[40:43], v210, v218 op_sel_hi:[0,0,0] cbsz:4 blgp:2
	buffer_load_dwordx4 v225, s[4:7], s36 offen lds
	v_mfma_scale_f32_16x16x128_f8f6f4 v[44:47], v[136:139], v[202:207], v[44:47], v210, v219 op_sel_hi:[0,0,0] cbsz:4 blgp:2
	s_add_u32 m0, s40, 0x4000
	v_mfma_scale_f32_16x16x128_f8f6f4 v[48:51], v[140:143], v[184:189], v[48:51], v211, v216 op_sel_hi:[0,0,0] cbsz:4 blgp:2
	ds_read_b128 v[166:169], v241 offset:1536
	v_mfma_scale_f32_16x16x128_f8f6f4 v[52:55], v[140:143], v[190:195], v[52:55], v211, v217 op_sel_hi:[0,0,0] cbsz:4 blgp:2
	buffer_load_dwordx4 v221, s[4:7], s37 offen lds
	v_mfma_scale_f32_16x16x128_f8f6f4 v[56:59], v[140:143], v[196:201], v[56:59], v211, v218 op_sel_hi:[0,0,0] cbsz:4 blgp:2
	s_add_u32 m0, s40, 0x6000
	v_mfma_scale_f32_16x16x128_f8f6f4 v[60:63], v[140:143], v[202:207], v[60:63], v211, v219 op_sel_hi:[0,0,0] cbsz:4 blgp:2
	ds_read_b64 v[170:171], v242 offset:1536
	v_mfma_scale_f32_16x16x128_f8f6f4 v[64:67], v[144:147], v[184:189], v[64:67], v212, v216 op_sel_hi:[0,0,0] cbsz:4 blgp:2
	buffer_load_dwordx4 v225, s[4:7], s37 offen lds
	v_mfma_scale_f32_16x16x128_f8f6f4 v[68:71], v[144:147], v[190:195], v[68:71], v212, v217 op_sel_hi:[0,0,0] cbsz:4 blgp:2
	s_add_u32 m0, s40, 0x8000
	v_mfma_scale_f32_16x16x128_f8f6f4 v[72:75], v[144:147], v[196:201], v[72:75], v212, v218 op_sel_hi:[0,0,0] cbsz:4 blgp:2
	ds_read_b128 v[172:175], v241 offset:3072
	v_mfma_scale_f32_16x16x128_f8f6f4 v[76:79], v[144:147], v[202:207], v[76:79], v212, v219 op_sel_hi:[0,0,0] cbsz:4 blgp:2
	buffer_load_dwordx4 v226, s[4:7], s37 offen lds
	v_mfma_scale_f32_16x16x128_f8f6f4 v[80:83], v[148:151], v[184:189], v[80:83], v213, v216 op_sel_hi:[0,0,0] cbsz:4 blgp:2
	ds_read_b64 v[176:177], v242 offset:3072
	v_mfma_scale_f32_16x16x128_f8f6f4 v[84:87], v[148:151], v[190:195], v[84:87], v213, v217 op_sel_hi:[0,0,0] cbsz:4 blgp:2
	ds_read_b128 v[178:181], v241 offset:4608
	v_mfma_scale_f32_16x16x128_f8f6f4 v[88:91], v[148:151], v[196:201], v[88:91], v213, v218 op_sel_hi:[0,0,0] cbsz:4 blgp:2
	ds_read_b64 v[182:183], v242 offset:4608
	v_mfma_scale_f32_16x16x128_f8f6f4 v[92:95], v[148:151], v[202:207], v[92:95], v213, v219 op_sel_hi:[0,0,0] cbsz:4 blgp:2
	s_add_u32 s36, s36, 0x4000
	v_mfma_scale_f32_16x16x128_f8f6f4 v[96:99], v[244:247], v[184:189], v[96:99], v214, v216 op_sel_hi:[0,0,0] cbsz:4 blgp:2
	s_add_u32 s37, s37, 0x6000
	v_mfma_scale_f32_16x16x128_f8f6f4 v[100:103], v[244:247], v[190:195], v[100:103], v214, v217 op_sel_hi:[0,0,0] cbsz:4 blgp:2
	s_add_u32 s40, s40, 0xa000
	v_mfma_scale_f32_16x16x128_f8f6f4 v[104:107], v[244:247], v[196:201], v[104:107], v214, v218 op_sel_hi:[0,0,0] cbsz:4 blgp:2
	s_sub_u32 s41, s40, 0x1e000
	v_mfma_scale_f32_16x16x128_f8f6f4 v[108:111], v[244:247], v[202:207], v[108:111], v214, v219 op_sel_hi:[0,0,0] cbsz:4 blgp:2
	s_cmp_ge_u32 s40, s49
	v_mfma_scale_f32_16x16x128_f8f6f4 v[112:115], v[252:255], v[184:189], v[112:115], v215, v216 op_sel_hi:[0,0,0] cbsz:4 blgp:2
	s_cselect_b32 s40, s41, s40
	v_mfma_scale_f32_16x16x128_f8f6f4 v[116:119], v[252:255], v[190:195], v[116:119], v215, v217 op_sel_hi:[0,0,0] cbsz:4 blgp:2
	ds_read_b128 v[128:131], v240 offset:0
	v_mfma_scale_f32_16x16x128_f8f6f4 v[120:123], v[252:255], v[196:201], v[120:123], v215, v218 op_sel_hi:[0,0,0] cbsz:4 blgp:2
	ds_read_b128 v[132:135], v240 offset:1024
	v_mfma_scale_f32_16x16x128_f8f6f4 v[124:127], v[252:255], v[202:207], v[124:127], v215, v219 op_sel_hi:[0,0,0] cbsz:4 blgp:2
	ds_read_b128 v[136:139], v240 offset:2048
	ds_read_b128 v[140:143], v240 offset:3072
	ds_read_b128 v[144:147], v240 offset:4096
	ds_read_b128 v[148:151], v240 offset:5120
	s_cmp_eq_u32 s34, 13
	s_cbranch_scc0 .Lnosc_or1
	s_add_u32 s44, s23, 1
	s_and_b32 s44, s44, 1
	s_cmp_lt_u32 s18, 4
	s_cselect_b32 s80, s26, s27
	s_cselect_b32 s82, s8, s10
	s_cselect_b32 s83, s9, s11
	s_lshl_b32 s80, s80, 10
	s_and_b32 s84, s18, 3
	s_lshl_b32 s84, s84, 8
	s_add_u32 s80, s80, s84
	s_add_u32 s82, s82, s80
	s_addc_u32 s83, s83, 0
	s_lshl_b32 s84, s44, 11
	s_lshl_b32 s85, s18, 8
	s_add_u32 s84, s84, s85
	s_add_u32 s84, s84, 0x1e000
	s_mov_b32 m0, s84
	v_lshlrev_b32_e32 v236, 2, v220
	global_load_lds_dword v236, s[82:83]
